# P1 and P10 row-loop stores made agent-scope write-through (sc1) so the L2 write-back at the following seam has less dirty data
# speedup vs baseline: 1.0046x; 1.0041x over previous
.Lp1_head:
	v_mul_f32_e32 v154, v127, v127
	v_mul_f32_e32 v155, v123, v123
	v_fmac_f32_e32 v154, v126, v126
	v_fmac_f32_e32 v155, v122, v122
	v_fmac_f32_e32 v154, v128, v128
	v_fmac_f32_e32 v155, v124, v124
	v_fmac_f32_e32 v154, v129, v129
	v_fmac_f32_e32 v155, v125, v125
	v_add_f32_e32 v154, v154, v155
	v_mul_f32_e32 v155, v119, v119
	v_fmac_f32_e32 v155, v118, v118
	v_fmac_f32_e32 v155, v120, v120
	v_fmac_f32_e32 v155, v121, v121
	v_add_f32_e32 v154, v155, v154
	v_mul_f32_e32 v155, v115, v115
	v_fmac_f32_e32 v155, v114, v114
	v_fmac_f32_e32 v155, v116, v116
	v_fmac_f32_e32 v155, v117, v117
	v_add_f32_e32 v154, v155, v154
	v_mul_f32_e32 v155, v111, v111
	v_fmac_f32_e32 v155, v110, v110
	v_fmac_f32_e32 v155, v112, v112
	v_fmac_f32_e32 v155, v113, v113
	v_add_f32_e32 v154, v155, v154
	v_mul_f32_e32 v155, v107, v107
	v_fmac_f32_e32 v155, v106, v106
	v_fmac_f32_e32 v155, v108, v108
	v_fmac_f32_e32 v155, v109, v109
	v_add_f32_e32 v154, v155, v154
	v_mul_f32_e32 v155, v103, v103
	v_fmac_f32_e32 v155, v102, v102
	v_fmac_f32_e32 v155, v104, v104
	v_fmac_f32_e32 v155, v105, v105
	v_add_f32_e32 v154, v155, v154
	v_mul_f32_e32 v155, v83, v83
	v_fmac_f32_e32 v155, v82, v82
	v_fmac_f32_e32 v155, v84, v84
	v_fmac_f32_e32 v155, v85, v85
	v_add_f32_e32 v154, v155, v154
	v_mov_b32_e32 v157, 0
	s_add_u32 s18, s18, 0x2000
	v_add_f32_dpp v154, v154, v154 quad_perm:[1,0,3,2] row_mask:0xf bank_mask:0xf bound_ctrl:1
	s_addc_u32 s19, s19, 0
	s_cmp_eq_u32 s18, 0x20000
	v_add_f32_dpp v154, v154, v154 quad_perm:[2,3,0,1] row_mask:0xf bank_mask:0xf bound_ctrl:1
	s_nop 1
	v_add_f32_dpp v154, v154, v154 row_half_mirror row_mask:0xf bank_mask:0xf bound_ctrl:1
	s_nop 1
	v_add_f32_dpp v154, v154, v154 row_mirror row_mask:0xf bank_mask:0xf bound_ctrl:1
	v_mov_b32_e32 v155, v154
	s_nop 1
	v_permlane16_swap_b32_e32 v154, v155
	v_add_f32_e32 v154, v154, v155
	v_mov_b32_e32 v155, v154
	s_nop 1
	v_permlane32_swap_b32_e32 v154, v155
	v_add_f32_e32 v154, v154, v155
	v_fmamk_f32 v154, v154, 0x3a000000, v152
	v_mul_f32_e32 v155, 0x4b800000, v154
	v_cmp_gt_f32_e32 vcc, s21, v154
	s_nop 1
	v_cndmask_b32_e32 v154, v154, v155, vcc
	v_rsq_f32_e32 v154, v154
	s_nop 0
	v_mul_f32_e32 v155, 0x45800000, v154
	v_cndmask_b32_e32 v154, v154, v155, vcc
	v_pk_mul_f32 v[126:127], v[126:127], v[154:155] op_sel_hi:[1,0]
	v_pk_mul_f32 v[128:129], v[128:129], v[154:155] op_sel_hi:[1,0]
	s_waitcnt lgkmcnt(13)
	v_pk_fma_f32 v[126:127], v[34:35], v[126:127], v[42:43]
	v_pk_fma_f32 v[128:129], v[36:37], v[128:129], v[44:45]
	v_med3_f32 v155, v126, s22, v153
	v_med3_f32 v156, v127, s22, v153
	v_cvt_pk_fp8_f32 v157, v155, v156
	v_med3_f32 v155, v128, s22, v153
	v_med3_f32 v156, v129, s22, v153
	v_pk_mul_f32 v[122:123], v[122:123], v[154:155] op_sel_hi:[1,0]
	v_cvt_pk_fp8_f32 v157, v155, v156 op_sel:[0,0,1]
	v_cvt_pk_bf16_f32 v126, v126, v127
	v_cvt_pk_bf16_f32 v127, v128, v129
	s_waitcnt lgkmcnt(12)
	v_pk_fma_f32 v[122:123], v[122:123], v[38:39], v[46:47]
	global_store_dwordx2 v[146:147], v[126:127], off offset:-2048 sc1
	global_store_dword v[148:149], v157, off offset:-1024 sc1
	v_med3_f32 v126, v122, s22, v153
	v_med3_f32 v127, v123, s22, v153
	v_mov_b32_e32 v128, 0
	v_cvt_pk_fp8_f32 v128, v126, v127
	v_pk_mul_f32 v[124:125], v[124:125], v[154:155] op_sel_hi:[1,0]
	v_pk_mul_f32 v[118:119], v[118:119], v[154:155] op_sel_hi:[1,0]
	v_pk_fma_f32 v[124:125], v[124:125], v[40:41], v[48:49]
	v_cvt_pk_bf16_f32 v122, v122, v123
	v_med3_f32 v126, v124, s22, v153
	v_med3_f32 v127, v125, s22, v153
	v_cvt_pk_fp8_f32 v128, v126, v127 op_sel:[0,0,1]
	v_cvt_pk_bf16_f32 v123, v124, v125
	s_waitcnt lgkmcnt(9)
	v_pk_fma_f32 v[118:119], v[118:119], v[50:51], v[58:59]
	global_store_dwordx2 v[146:147], v[122:123], off offset:-1536 sc1
	global_store_dword v[148:149], v128, off offset:-768 sc1
	v_med3_f32 v122, v118, s22, v153
	v_med3_f32 v123, v119, s22, v153
	v_mov_b32_e32 v124, 0
	v_cvt_pk_fp8_f32 v124, v122, v123
	v_pk_mul_f32 v[120:121], v[120:121], v[154:155] op_sel_hi:[1,0]
	v_pk_mul_f32 v[114:115], v[114:115], v[154:155] op_sel_hi:[1,0]
	v_pk_fma_f32 v[120:121], v[120:121], v[52:53], v[60:61]
	v_cvt_pk_bf16_f32 v118, v118, v119
	v_med3_f32 v122, v120, s22, v153
	v_med3_f32 v123, v121, s22, v153
	v_cvt_pk_fp8_f32 v124, v122, v123 op_sel:[0,0,1]
	v_cvt_pk_bf16_f32 v119, v120, v121
	s_waitcnt lgkmcnt(8)
	v_pk_fma_f32 v[114:115], v[114:115], v[54:55], v[62:63]
	global_store_dwordx2 v[146:147], v[118:119], off offset:-1024 sc1
	global_store_dword v[148:149], v124, off offset:-512 sc1
	v_med3_f32 v118, v114, s22, v153
	v_med3_f32 v119, v115, s22, v153
	v_mov_b32_e32 v120, 0
	v_cvt_pk_fp8_f32 v120, v118, v119
	v_pk_mul_f32 v[116:117], v[116:117], v[154:155] op_sel_hi:[1,0]
	v_pk_mul_f32 v[110:111], v[110:111], v[154:155] op_sel_hi:[1,0]
	v_pk_fma_f32 v[116:117], v[116:117], v[56:57], v[64:65]
	v_cvt_pk_bf16_f32 v114, v114, v115
	v_med3_f32 v118, v116, s22, v153
	v_med3_f32 v119, v117, s22, v153
	v_cvt_pk_fp8_f32 v120, v118, v119 op_sel:[0,0,1]
	v_cvt_pk_bf16_f32 v115, v116, v117
	s_waitcnt lgkmcnt(5)
	v_pk_fma_f32 v[110:111], v[110:111], v[66:67], v[74:75]
	global_store_dwordx2 v[146:147], v[114:115], off offset:-512 sc1
	global_store_dword v[148:149], v120, off offset:-256 sc1
	v_med3_f32 v114, v110, s22, v153
	v_med3_f32 v115, v111, s22, v153
	v_mov_b32_e32 v116, 0
	v_cvt_pk_fp8_f32 v116, v114, v115
	v_pk_mul_f32 v[112:113], v[112:113], v[154:155] op_sel_hi:[1,0]
	v_pk_mul_f32 v[106:107], v[106:107], v[154:155] op_sel_hi:[1,0]
	v_pk_fma_f32 v[112:113], v[112:113], v[68:69], v[76:77]
	v_cvt_pk_bf16_f32 v110, v110, v111
	v_med3_f32 v114, v112, s22, v153
	v_med3_f32 v115, v113, s22, v153
	v_cvt_pk_fp8_f32 v116, v114, v115 op_sel:[0,0,1]
	v_cvt_pk_bf16_f32 v111, v112, v113
	s_waitcnt lgkmcnt(4)
	v_pk_fma_f32 v[106:107], v[106:107], v[70:71], v[78:79]
	global_store_dwordx2 v[146:147], v[110:111], off sc1
	global_store_dword v[148:149], v116, off sc1
	v_med3_f32 v110, v106, s22, v153
	v_med3_f32 v111, v107, s22, v153
	v_mov_b32_e32 v112, 0
	v_cvt_pk_fp8_f32 v112, v110, v111
	v_pk_mul_f32 v[108:109], v[108:109], v[154:155] op_sel_hi:[1,0]
	v_pk_mul_f32 v[102:103], v[102:103], v[154:155] op_sel_hi:[1,0]
	v_pk_fma_f32 v[108:109], v[108:109], v[72:73], v[80:81]
	v_cvt_pk_bf16_f32 v106, v106, v107
	v_med3_f32 v110, v108, s22, v153
	v_med3_f32 v111, v109, s22, v153
	v_cvt_pk_fp8_f32 v112, v110, v111 op_sel:[0,0,1]
	v_cvt_pk_bf16_f32 v107, v108, v109
	s_waitcnt lgkmcnt(1)
	v_pk_fma_f32 v[102:103], v[102:103], v[86:87], v[94:95]
	global_store_dwordx2 v[146:147], v[106:107], off offset:512 sc1
	global_store_dword v[148:149], v112, off offset:256 sc1
	v_med3_f32 v106, v102, s22, v153
	v_med3_f32 v107, v103, s22, v153
	v_mov_b32_e32 v108, 0
	v_cvt_pk_fp8_f32 v108, v106, v107
	v_pk_mul_f32 v[104:105], v[104:105], v[154:155] op_sel_hi:[1,0]
	v_pk_mul_f32 v[82:83], v[82:83], v[154:155] op_sel_hi:[1,0]
	v_pk_fma_f32 v[104:105], v[104:105], v[88:89], v[96:97]
	v_cvt_pk_bf16_f32 v102, v102, v103
	v_med3_f32 v106, v104, s22, v153
	v_med3_f32 v107, v105, s22, v153
	v_cvt_pk_fp8_f32 v108, v106, v107 op_sel:[0,0,1]
	v_cvt_pk_bf16_f32 v103, v104, v105
	s_waitcnt lgkmcnt(0)
	v_pk_fma_f32 v[82:83], v[82:83], v[90:91], v[98:99]
	global_store_dwordx2 v[146:147], v[102:103], off offset:1024 sc1
	global_store_dword v[148:149], v108, off offset:512 sc1
	v_med3_f32 v102, v82, s22, v153
	v_med3_f32 v103, v83, s22, v153
	v_mov_b32_e32 v104, 0
	v_cvt_pk_fp8_f32 v104, v102, v103
	v_pk_mul_f32 v[84:85], v[84:85], v[154:155] op_sel_hi:[1,0]
	v_cvt_pk_bf16_f32 v82, v82, v83
	v_pk_fma_f32 v[84:85], v[84:85], v[92:93], v[100:101]
	s_nop 0
	v_med3_f32 v102, v84, s22, v153
	v_med3_f32 v103, v85, s22, v153
	v_cvt_pk_fp8_f32 v104, v102, v103 op_sel:[0,0,1]
	v_cvt_pk_bf16_f32 v83, v84, v85
	global_store_dwordx2 v[146:147], v[82:83], off offset:1536 sc1
	global_store_dword v[148:149], v104, off offset:768 sc1
	v_lshl_add_u64 v[148:149], v[148:149], 0, s[12:13]
	v_lshl_add_u64 v[146:147], v[146:147], 0, s[14:15]
	s_cbranch_scc1 .LBB0_99
	s_waitcnt vmcnt(16)
	v_mov_b32_e32 v126, v14
	v_mov_b32_e32 v127, v15
	v_mov_b32_e32 v128, v16
	v_mov_b32_e32 v129, v17
	v_mov_b32_e32 v122, v10
	v_mov_b32_e32 v123, v11
	v_mov_b32_e32 v124, v12
	v_mov_b32_e32 v125, v13
	v_mov_b32_e32 v118, v6
	v_mov_b32_e32 v119, v7
	v_mov_b32_e32 v120, v8
	v_mov_b32_e32 v121, v9
	v_mov_b32_e32 v114, v2
	v_mov_b32_e32 v115, v3
	v_mov_b32_e32 v116, v4
	v_mov_b32_e32 v117, v5
	v_mov_b32_e32 v110, v30
	v_mov_b32_e32 v111, v31
	v_mov_b32_e32 v112, v32
	v_mov_b32_e32 v113, v33
	v_mov_b32_e32 v106, v26
	v_mov_b32_e32 v107, v27
	v_mov_b32_e32 v108, v28
	v_mov_b32_e32 v109, v29
	v_mov_b32_e32 v102, v22
	v_mov_b32_e32 v103, v23
	v_mov_b32_e32 v104, v24
	v_mov_b32_e32 v105, v25
	v_mov_b32_e32 v82, v18
	v_mov_b32_e32 v83, v19
	v_mov_b32_e32 v84, v20
	v_mov_b32_e32 v85, v21
	s_cmp_eq_u32 s18, 0x1e000
	s_cbranch_scc0 .Lp1_issue
	s_branch .Lp1_head

.Lp10_head:
	v_lshlrev_b32_e32 v154, 16, v120
	v_and_b32_e32 v155, 0xffff0000, v120
	v_lshlrev_b32_e32 v152, 16, v121
	v_and_b32_e32 v153, 0xffff0000, v121
	v_pk_mul_f32 v[146:147], v[154:155], v[154:155]
	v_pk_mul_f32 v[144:145], v[152:153], v[152:153]
	v_lshlrev_b32_e32 v158, 16, v118
	v_and_b32_e32 v159, 0xffff0000, v118
	v_add_f32_e32 v146, v146, v147
	v_lshlrev_b32_e32 v156, 16, v119
	v_and_b32_e32 v157, 0xffff0000, v119
	v_pk_mul_f32 v[150:151], v[158:159], v[158:159]
	v_add_f32_e32 v144, v144, v146
	v_pk_mul_f32 v[148:149], v[156:157], v[156:157]
	v_add_f32_e32 v144, v145, v144
	v_add_f32_e32 v145, v150, v151
	v_lshlrev_b32_e32 v164, 16, v116
	v_and_b32_e32 v165, 0xffff0000, v116
	v_add_f32_e32 v145, v148, v145
	v_lshlrev_b32_e32 v160, 16, v117
	v_and_b32_e32 v161, 0xffff0000, v117
	v_pk_mul_f32 v[166:167], v[164:165], v[164:165]
	v_add_f32_e32 v145, v149, v145
	v_pk_mul_f32 v[162:163], v[160:161], v[160:161]
	v_add_f32_e32 v144, v145, v144
	v_add_f32_e32 v145, v166, v167
	v_lshlrev_b32_e32 v172, 16, v114
	v_and_b32_e32 v173, 0xffff0000, v114
	v_add_f32_e32 v145, v162, v145
	v_lshlrev_b32_e32 v168, 16, v115
	v_and_b32_e32 v169, 0xffff0000, v115
	v_pk_mul_f32 v[174:175], v[172:173], v[172:173]
	v_lshlrev_b32_e32 v180, 16, v112
	v_and_b32_e32 v181, 0xffff0000, v112
	v_add_f32_e32 v145, v163, v145
	v_pk_mul_f32 v[170:171], v[168:169], v[168:169]
	v_lshlrev_b32_e32 v176, 16, v113
	v_and_b32_e32 v177, 0xffff0000, v113
	v_pk_mul_f32 v[112:113], v[180:181], v[180:181]
	v_lshlrev_b32_e32 v186, 16, v110
	v_and_b32_e32 v187, 0xffff0000, v110
	v_add_f32_e32 v144, v145, v144
	v_add_f32_e32 v145, v174, v175
	v_pk_mul_f32 v[178:179], v[176:177], v[176:177]
	v_lshlrev_b32_e32 v182, 16, v111
	v_and_b32_e32 v183, 0xffff0000, v111
	v_pk_mul_f32 v[110:111], v[186:187], v[186:187]
	v_lshlrev_b32_e32 v192, 16, v108
	v_and_b32_e32 v193, 0xffff0000, v108
	v_add_f32_e32 v145, v170, v145
	v_add_f32_e32 v112, v112, v113
	v_pk_mul_f32 v[184:185], v[182:183], v[182:183]
	v_lshlrev_b32_e32 v188, 16, v109
	v_and_b32_e32 v189, 0xffff0000, v109
	v_pk_mul_f32 v[108:109], v[192:193], v[192:193]
	v_lshlrev_b32_e32 v198, 16, v106
	v_and_b32_e32 v199, 0xffff0000, v106
	v_add_f32_e32 v145, v171, v145
	v_add_f32_e32 v112, v178, v112
	v_add_f32_e32 v110, v110, v111
	v_pk_mul_f32 v[190:191], v[188:189], v[188:189]
	v_lshlrev_b32_e32 v194, 16, v107
	v_and_b32_e32 v195, 0xffff0000, v107
	v_pk_mul_f32 v[106:107], v[198:199], v[198:199]
	v_add_f32_e32 v144, v145, v144
	v_add_f32_e32 v112, v179, v112
	v_add_f32_e32 v110, v184, v110
	v_add_f32_e32 v108, v108, v109
	v_pk_mul_f32 v[196:197], v[194:195], v[194:195]
	v_add_f32_e32 v112, v112, v144
	v_add_f32_e32 v110, v185, v110
	v_add_f32_e32 v108, v190, v108
	v_add_f32_e32 v106, v106, v107
	v_add_f32_e32 v110, v110, v112
	v_add_f32_e32 v108, v191, v108
	v_add_f32_e32 v106, v196, v106
	v_add_f32_e32 v108, v108, v110
	v_add_f32_e32 v106, v197, v106
	v_add_f32_e32 v106, v106, v108
	v_add_u32_e32 v135, 0, v72
	ds_read_b128 v[118:121], v135
	ds_read_b128 v[136:139], v135 offset:1024
	v_add_f32_dpp v106, v106, v106 quad_perm:[1,0,3,2] row_mask:0xf bank_mask:0xf bound_ctrl:1
	ds_read_b128 v[114:117], v135 offset:2048
	ds_read_b128 v[140:143], v135 offset:3072
	v_add_f32_dpp v106, v106, v106 quad_perm:[2,3,0,1] row_mask:0xf bank_mask:0xf bound_ctrl:1
	s_add_u32 s56, s14, s10
	s_addc_u32 s57, s15, s11
	v_add_f32_dpp v106, v106, v106 row_half_mirror row_mask:0xf bank_mask:0xf bound_ctrl:1
	s_add_u32 s10, s10, 0x1000
	s_addc_u32 s11, s11, 0
	v_add_f32_dpp v106, v106, v106 row_mirror row_mask:0xf bank_mask:0xf bound_ctrl:1
	v_mov_b32_e32 v107, v106
	s_nop 1
	v_permlane16_swap_b32_e32 v106, v107
	v_add_f32_e32 v106, v106, v107
	v_mov_b32_e32 v107, v106
	s_nop 1
	v_permlane32_swap_b32_e32 v106, v107
	v_add_f32_e32 v106, v106, v107
	v_fmamk_f32 v106, v106, 0x3a000000, v126
	v_mul_f32_e32 v107, 0x4b800000, v106
	v_cmp_gt_f32_e32 vcc, s62, v106
	v_lshl_add_u64 v[104:105], v[104:105], 0, s[30:31]
	s_nop 0
	v_cndmask_b32_e32 v106, v106, v107, vcc
	v_rsq_f32_e32 v162, v106
	ds_read_b128 v[106:109], v135 offset:4096
	ds_read_b128 v[110:113], v135 offset:5120
	ds_read_b128 v[144:147], v135 offset:6144
	ds_read_b128 v[148:151], v135 offset:7168
	v_mul_f32_e32 v135, 0x45800000, v162
	v_cndmask_b32_e32 v162, v162, v135, vcc
	v_pk_mul_f32 v[154:155], v[162:163], v[154:155] op_sel_hi:[0,1]
	s_waitcnt lgkmcnt(7)
	v_pk_fma_f32 v[118:119], v[118:119], v[154:155], v[62:63]
	v_pk_mul_f32 v[62:63], v[162:163], v[152:153] op_sel_hi:[0,1]
	v_pk_fma_f32 v[120:121], v[120:121], v[62:63], v[64:65]
	v_add_co_u32_e32 v122, vcc, s63, v122
	v_pk_mul_f32 v[154:155], v[118:119], v[118:119]
	v_cvt_pk_bf16_f32 v62, v118, v119
	v_cvt_pk_bf16_f32 v63, v120, v121
	v_addc_co_u32_e32 v123, vcc, 0, v123, vcc
	v_pk_mul_f32 v[152:153], v[120:121], v[120:121]
	global_store_dwordx2 v[122:123], v[62:63], off sc1
	v_pk_mul_f32 v[62:63], v[162:163], v[158:159] op_sel_hi:[0,1]
	v_add_f32_e32 v135, v154, v155
	s_waitcnt lgkmcnt(6)
	v_pk_fma_f32 v[136:137], v[136:137], v[62:63], v[58:59]
	v_pk_mul_f32 v[58:59], v[162:163], v[156:157] op_sel_hi:[0,1]
	v_add_f32_e32 v135, v152, v135
	v_pk_mul_f32 v[158:159], v[136:137], v[136:137]
	v_pk_fma_f32 v[138:139], v[138:139], v[58:59], v[60:61]
	v_add_f32_e32 v135, v153, v135
	v_cvt_pk_bf16_f32 v58, v136, v137
	v_cvt_pk_bf16_f32 v59, v138, v139
	v_add_f32_e32 v135, v158, v135
	v_pk_mul_f32 v[156:157], v[138:139], v[138:139]
	global_store_dwordx2 v[122:123], v[58:59], off offset:512 sc1
	v_pk_mul_f32 v[58:59], v[162:163], v[164:165] op_sel_hi:[0,1]
	v_add_f32_e32 v135, v159, v135
	s_waitcnt lgkmcnt(5)
	v_pk_fma_f32 v[64:65], v[58:59], v[114:115], v[54:55]
	v_pk_mul_f32 v[54:55], v[162:163], v[160:161] op_sel_hi:[0,1]
	v_add_f32_e32 v135, v156, v135
	v_pk_mul_f32 v[114:115], v[64:65], v[64:65]
	v_pk_fma_f32 v[62:63], v[54:55], v[116:117], v[56:57]
	v_add_f32_e32 v135, v157, v135
	v_cvt_pk_bf16_f32 v54, v64, v65
	v_cvt_pk_bf16_f32 v55, v62, v63
	v_add_f32_e32 v114, v114, v135
	v_pk_mul_f32 v[116:117], v[62:63], v[62:63]
	global_store_dwordx2 v[122:123], v[54:55], off offset:1024 sc1
	v_pk_mul_f32 v[54:55], v[162:163], v[172:173] op_sel_hi:[0,1]
	v_add_f32_e32 v114, v115, v114
	s_waitcnt lgkmcnt(4)
	v_pk_fma_f32 v[60:61], v[54:55], v[140:141], v[14:15]
	v_pk_mul_f32 v[14:15], v[162:163], v[168:169] op_sel_hi:[0,1]
	v_add_f32_e32 v114, v116, v114
	v_pk_mul_f32 v[140:141], v[60:61], v[60:61]
	v_pk_fma_f32 v[58:59], v[14:15], v[142:143], v[16:17]
	v_add_f32_e32 v114, v117, v114
	v_cvt_pk_bf16_f32 v14, v60, v61
	v_cvt_pk_bf16_f32 v15, v58, v59
	v_add_f32_e32 v114, v140, v114
	v_pk_mul_f32 v[16:17], v[58:59], v[58:59]
	global_store_dwordx2 v[122:123], v[14:15], off offset:1536 sc1
	v_pk_mul_f32 v[14:15], v[162:163], v[180:181] op_sel_hi:[0,1]
	v_add_f32_e32 v114, v141, v114
	s_waitcnt lgkmcnt(3)
	v_pk_fma_f32 v[56:57], v[14:15], v[106:107], v[50:51]
	v_pk_mul_f32 v[14:15], v[162:163], v[176:177] op_sel_hi:[0,1]
	v_add_f32_e32 v16, v16, v114
	v_pk_mul_f32 v[50:51], v[56:57], v[56:57]
	v_pk_fma_f32 v[54:55], v[14:15], v[108:109], v[52:53]
	v_add_f32_e32 v16, v17, v16
	v_cvt_pk_bf16_f32 v14, v56, v57
	v_cvt_pk_bf16_f32 v15, v54, v55
	v_add_f32_e32 v16, v50, v16
	v_pk_mul_f32 v[106:107], v[54:55], v[54:55]
	global_store_dwordx2 v[122:123], v[14:15], off offset:2048 sc1
	v_pk_mul_f32 v[14:15], v[162:163], v[186:187] op_sel_hi:[0,1]
	v_add_f32_e32 v16, v51, v16
	s_waitcnt lgkmcnt(2)
	v_pk_fma_f32 v[52:53], v[14:15], v[110:111], v[10:11]
	v_pk_mul_f32 v[10:11], v[162:163], v[182:183] op_sel_hi:[0,1]
	v_add_f32_e32 v16, v106, v16
	v_pk_mul_f32 v[108:109], v[52:53], v[52:53]
	v_pk_fma_f32 v[14:15], v[10:11], v[112:113], v[12:13]
	v_add_f32_e32 v16, v107, v16
	v_cvt_pk_bf16_f32 v10, v52, v53
	v_cvt_pk_bf16_f32 v11, v14, v15
	v_add_f32_e32 v16, v108, v16
	v_pk_mul_f32 v[12:13], v[14:15], v[14:15]
	global_store_dwordx2 v[122:123], v[10:11], off offset:2560 sc1
	v_pk_mul_f32 v[10:11], v[162:163], v[192:193] op_sel_hi:[0,1]
	v_add_f32_e32 v16, v109, v16
	s_waitcnt lgkmcnt(1)
	v_pk_fma_f32 v[10:11], v[10:11], v[144:145], v[6:7]
	v_pk_mul_f32 v[6:7], v[162:163], v[188:189] op_sel_hi:[0,1]
	v_add_f32_e32 v12, v12, v16
	v_pk_mul_f32 v[110:111], v[10:11], v[10:11]
	v_pk_fma_f32 v[8:9], v[6:7], v[146:147], v[8:9]
	v_add_f32_e32 v12, v13, v12
	v_cvt_pk_bf16_f32 v6, v10, v11
	v_cvt_pk_bf16_f32 v7, v8, v9
	v_add_f32_e32 v12, v110, v12
	v_pk_mul_f32 v[112:113], v[8:9], v[8:9]
	global_store_dwordx2 v[122:123], v[6:7], off offset:3072 sc1
	v_pk_mul_f32 v[6:7], v[162:163], v[198:199] op_sel_hi:[0,1]
	v_add_f32_e32 v12, v111, v12
	s_waitcnt lgkmcnt(0)
	v_pk_fma_f32 v[6:7], v[6:7], v[148:149], v[2:3]
	v_add_f32_e32 v12, v112, v12
	v_pk_mul_f32 v[142:143], v[6:7], v[6:7]
	v_pk_mul_f32 v[2:3], v[162:163], v[194:195] op_sel_hi:[0,1]
	v_add_f32_e32 v12, v113, v12
	v_pk_fma_f32 v[2:3], v[2:3], v[150:151], v[4:5]
	v_add_f32_e32 v12, v142, v12
	v_pk_mul_f32 v[4:5], v[2:3], v[2:3]
	v_add_f32_e32 v12, v143, v12
	v_add_f32_e32 v4, v4, v12
	v_add_f32_e32 v4, v5, v4
	v_mov_b32_e32 v50, v124
	v_mov_b32_e32 v114, 0
	v_add_f32_dpp v4, v4, v4 quad_perm:[1,0,3,2] row_mask:0xf bank_mask:0xf bound_ctrl:1
	s_nop 1
	v_add_f32_dpp v4, v4, v4 quad_perm:[2,3,0,1] row_mask:0xf bank_mask:0xf bound_ctrl:1
	s_nop 1
	v_add_f32_dpp v4, v4, v4 row_half_mirror row_mask:0xf bank_mask:0xf bound_ctrl:1
	s_nop 1
	v_add_f32_dpp v4, v4, v4 row_mirror row_mask:0xf bank_mask:0xf bound_ctrl:1
	v_mov_b32_e32 v5, v4
	s_nop 1
	v_permlane16_swap_b32_e32 v4, v5
	v_add_f32_e32 v4, v4, v5
	v_mov_b32_e32 v5, v4
	s_nop 1
	v_permlane32_swap_b32_e32 v4, v5
	v_add_f32_e32 v4, v4, v5
	v_fmamk_f32 v4, v4, 0x3a000000, v126
	v_mul_f32_e32 v5, 0x4b800000, v4
	v_cmp_gt_f32_e32 vcc, s62, v4
	s_nop 1
	v_cndmask_b32_e32 v4, v4, v5, vcc
	v_rsq_f32_e32 v12, v4
	v_cvt_pk_bf16_f32 v4, v6, v7
	v_cvt_pk_bf16_f32 v5, v2, v3
	global_store_dwordx2 v[122:123], v[4:5], off offset:3584 sc1
	v_mul_f32_e32 v4, 0x45800000, v12
	v_lshl_add_u32 v5, v50, 2, 0
	v_add_u32_e32 v16, 0x4000, v5
	v_add_u32_e32 v51, 0x6000, v5
	ds_read2_b32 v[16:17], v16 offset1:1
	ds_read2_b32 v[106:107], v51 offset1:1
	v_add_u32_e32 v51, 0x4008, v5
	v_add_u32_e32 v110, 0x6008, v5
	v_cndmask_b32_e32 v4, v12, v4, vcc
	ds_read2_b32 v[108:109], v51 offset1:1
	ds_read2_b32 v[110:111], v110 offset1:1
	v_pk_mul_f32 v[12:13], v[118:119], v[4:5] op_sel_hi:[1,0]
	v_pk_mul_f32 v[112:113], v[120:121], v[4:5] op_sel_hi:[1,0]
	s_waitcnt lgkmcnt(2)
	v_pk_fma_f32 v[16:17], v[16:17], v[12:13], v[106:107]
	v_pk_mul_f32 v[116:117], v[138:139], v[4:5] op_sel_hi:[1,0]
	v_cvt_pk_bf16_f32 v51, v16, 0
	v_cvt_pk_bf16_f32 v12, v17, 0
	v_lshlrev_b32_e32 v13, 16, v12
	v_lshlrev_b32_e32 v12, 16, v51
	v_pk_add_f32 v[106:107], v[16:17], v[12:13] neg_lo:[0,1] neg_hi:[0,1]
	s_waitcnt lgkmcnt(0)
	v_pk_fma_f32 v[108:109], v[108:109], v[112:113], v[110:111]
	v_med3_f32 v16, v16, s68, v132
	v_med3_f32 v17, v17, s68, v132
	v_cvt_pk_bf16_f32 v12, v108, 0
	v_cvt_pk_bf16_f32 v110, v109, 0
	v_cvt_pk_fp8_f32 v114, v16, v17
	v_lshlrev_b32_e32 v111, 16, v110
	v_lshlrev_b32_e32 v110, 16, v12
	v_pk_add_f32 v[112:113], v[108:109], v[110:111] neg_lo:[0,1] neg_hi:[0,1]
	v_and_or_b32 v110, v51, s64, v13
	v_ashrrev_i32_e32 v51, 31, v50
	v_cvt_pk_bf16_f32 v106, v106, v107
	v_cvt_pk_bf16_f32 v107, v112, v113
	v_lshl_add_u64 v[112:113], v[50:51], 1, s[56:57]
	v_med3_f32 v16, v108, s68, v132
	v_med3_f32 v17, v109, s68, v132
	v_and_or_b32 v111, v12, s64, v111
	v_add_co_u32_e32 v12, vcc, s65, v112
	v_cvt_pk_fp8_f32 v114, v16, v17 op_sel:[0,0,1]
	s_nop 0
	v_addc_co_u32_e32 v13, vcc, 0, v113, vcc
	v_add_co_u32_e32 v16, vcc, s67, v112
	v_lshl_add_u64 v[50:51], s[12:13], 0, v[50:51]
	s_nop 0
	v_addc_co_u32_e32 v17, vcc, 0, v113, vcc
	global_store_dwordx2 v[12:13], v[110:111], off sc1
	global_store_dwordx2 v[16:17], v[106:107], off sc1
	global_store_dword v[50:51], v114, off offset:-1024 sc1
	v_add_u32_e32 v108, 0x4400, v5
	v_add_u32_e32 v110, 0x6400, v5
	ds_read2_b32 v[108:109], v108 offset1:1
	ds_read2_b32 v[110:111], v110 offset1:1
	v_add_u32_e32 v112, 0x4408, v5
	v_add_u32_e32 v114, 0x6408, v5
	ds_read2_b32 v[112:113], v112 offset1:1
	ds_read2_b32 v[114:115], v114 offset1:1
	v_pk_mul_f32 v[106:107], v[136:137], v[4:5] op_sel_hi:[1,0]
	v_pk_mul_f32 v[64:65], v[64:65], v[4:5] op_sel_hi:[1,0]
	s_waitcnt lgkmcnt(2)
	v_pk_fma_f32 v[106:107], v[106:107], v[108:109], v[110:111]
	v_pk_mul_f32 v[62:63], v[62:63], v[4:5] op_sel_hi:[1,0]
	v_cvt_pk_bf16_f32 v118, v106, 0
	v_cvt_pk_bf16_f32 v108, v107, 0
	v_lshlrev_b32_e32 v109, 16, v108
	v_lshlrev_b32_e32 v108, 16, v118
	s_waitcnt lgkmcnt(0)
	v_pk_fma_f32 v[112:113], v[116:117], v[112:113], v[114:115]
	v_pk_add_f32 v[110:111], v[106:107], v[108:109] neg_lo:[0,1] neg_hi:[0,1]
	v_cvt_pk_bf16_f32 v119, v112, 0
	v_cvt_pk_bf16_f32 v108, v113, 0
	v_lshlrev_b32_e32 v115, 16, v108
	v_lshlrev_b32_e32 v114, 16, v119
	v_pk_add_f32 v[116:117], v[112:113], v[114:115] neg_lo:[0,1] neg_hi:[0,1]
	v_med3_f32 v106, v106, s68, v132
	v_med3_f32 v107, v107, s68, v132
	v_mov_b32_e32 v114, 0
	v_cvt_pk_fp8_f32 v114, v106, v107
	v_cvt_pk_bf16_f32 v106, v110, v111
	v_med3_f32 v107, v112, s68, v132
	v_med3_f32 v110, v113, s68, v132
	v_cvt_pk_fp8_f32 v114, v107, v110 op_sel:[0,0,1]
	v_and_or_b32 v108, v118, s64, v109
	v_and_or_b32 v109, v119, s64, v115
	v_cvt_pk_bf16_f32 v107, v116, v117
	global_store_dwordx2 v[12:13], v[108:109], off offset:512 sc1
	global_store_dwordx2 v[16:17], v[106:107], off offset:512 sc1
	global_store_dword v[50:51], v114, off offset:-768 sc1
	v_add_u32_e32 v106, 0x4800, v5
	v_add_u32_e32 v108, 0x6800, v5
	ds_read2_b32 v[106:107], v106 offset1:1
	ds_read2_b32 v[108:109], v108 offset1:1
	v_add_u32_e32 v110, 0x4808, v5
	v_add_u32_e32 v112, 0x6808, v5
	ds_read2_b32 v[110:111], v110 offset1:1
	ds_read2_b32 v[112:113], v112 offset1:1
	v_pk_mul_f32 v[60:61], v[60:61], v[4:5] op_sel_hi:[1,0]
	s_waitcnt lgkmcnt(2)
	v_pk_fma_f32 v[64:65], v[64:65], v[106:107], v[108:109]
	v_pk_mul_f32 v[58:59], v[58:59], v[4:5] op_sel_hi:[1,0]
	v_cvt_pk_bf16_f32 v114, v64, 0
	v_cvt_pk_bf16_f32 v106, v65, 0
	v_lshlrev_b32_e32 v107, 16, v106
	v_lshlrev_b32_e32 v106, 16, v114
	s_waitcnt lgkmcnt(0)
	v_pk_fma_f32 v[62:63], v[62:63], v[110:111], v[112:113]
	v_pk_add_f32 v[108:109], v[64:65], v[106:107] neg_lo:[0,1] neg_hi:[0,1]
	v_cvt_pk_bf16_f32 v115, v62, 0
	v_cvt_pk_bf16_f32 v106, v63, 0
	v_lshlrev_b32_e32 v111, 16, v106
	v_lshlrev_b32_e32 v110, 16, v115
	v_pk_add_f32 v[112:113], v[62:63], v[110:111] neg_lo:[0,1] neg_hi:[0,1]
	v_med3_f32 v64, v64, s68, v132
	v_med3_f32 v65, v65, s68, v132
	v_mov_b32_e32 v110, 0
	v_cvt_pk_fp8_f32 v110, v64, v65
	v_med3_f32 v62, v62, s68, v132
	v_med3_f32 v63, v63, s68, v132
	v_and_or_b32 v106, v114, s64, v107
	v_cvt_pk_fp8_f32 v110, v62, v63 op_sel:[0,0,1]
	v_and_or_b32 v107, v115, s64, v111
	v_cvt_pk_bf16_f32 v64, v108, v109
	v_cvt_pk_bf16_f32 v65, v112, v113
	global_store_dwordx2 v[12:13], v[106:107], off offset:1024 sc1
	global_store_dwordx2 v[16:17], v[64:65], off offset:1024 sc1
	global_store_dword v[50:51], v110, off offset:-512 sc1
	v_add_u32_e32 v62, 0x4c00, v5
	v_add_u32_e32 v64, 0x6c00, v5
	ds_read2_b32 v[62:63], v62 offset1:1
	ds_read2_b32 v[64:65], v64 offset1:1
	v_add_u32_e32 v106, 0x4c08, v5
	v_add_u32_e32 v108, 0x6c08, v5
	ds_read2_b32 v[106:107], v106 offset1:1
	ds_read2_b32 v[108:109], v108 offset1:1
	v_pk_mul_f32 v[56:57], v[56:57], v[4:5] op_sel_hi:[1,0]
	s_waitcnt lgkmcnt(2)
	v_pk_fma_f32 v[60:61], v[60:61], v[62:63], v[64:65]
	v_pk_mul_f32 v[54:55], v[54:55], v[4:5] op_sel_hi:[1,0]
	v_cvt_pk_bf16_f32 v110, v60, 0
	v_cvt_pk_bf16_f32 v62, v61, 0
	v_lshlrev_b32_e32 v63, 16, v62
	v_lshlrev_b32_e32 v62, 16, v110
	s_waitcnt lgkmcnt(0)
	v_pk_fma_f32 v[58:59], v[58:59], v[106:107], v[108:109]
	v_pk_add_f32 v[64:65], v[60:61], v[62:63] neg_lo:[0,1] neg_hi:[0,1]
	v_cvt_pk_bf16_f32 v111, v58, 0
	v_cvt_pk_bf16_f32 v62, v59, 0
	v_lshlrev_b32_e32 v107, 16, v62
	v_lshlrev_b32_e32 v106, 16, v111
	v_pk_add_f32 v[108:109], v[58:59], v[106:107] neg_lo:[0,1] neg_hi:[0,1]
	v_med3_f32 v60, v60, s68, v132
	v_med3_f32 v61, v61, s68, v132
	v_mov_b32_e32 v106, 0
	v_cvt_pk_fp8_f32 v106, v60, v61
	v_med3_f32 v58, v58, s68, v132
	v_med3_f32 v59, v59, s68, v132
	v_and_or_b32 v62, v110, s64, v63
	v_cvt_pk_fp8_f32 v106, v58, v59 op_sel:[0,0,1]
	v_and_or_b32 v63, v111, s64, v107
	v_cvt_pk_bf16_f32 v60, v64, v65
	v_cvt_pk_bf16_f32 v61, v108, v109
	global_store_dwordx2 v[12:13], v[62:63], off offset:1536 sc1
	global_store_dwordx2 v[16:17], v[60:61], off offset:1536 sc1
	global_store_dword v[50:51], v106, off offset:-256 sc1
	v_add_u32_e32 v58, 0x5000, v5
	v_add_u32_e32 v60, 0x7000, v5
	ds_read2_b32 v[58:59], v58 offset1:1
	ds_read2_b32 v[60:61], v60 offset1:1
	v_add_u32_e32 v62, 0x5008, v5
	v_add_u32_e32 v64, 0x7008, v5
	ds_read2_b32 v[62:63], v62 offset1:1
	ds_read2_b32 v[64:65], v64 offset1:1
	v_pk_mul_f32 v[52:53], v[52:53], v[4:5] op_sel_hi:[1,0]
	s_waitcnt lgkmcnt(2)
	v_pk_fma_f32 v[56:57], v[56:57], v[58:59], v[60:61]
	v_pk_mul_f32 v[14:15], v[14:15], v[4:5] op_sel_hi:[1,0]
	v_cvt_pk_bf16_f32 v106, v56, 0
	v_cvt_pk_bf16_f32 v58, v57, 0
	v_lshlrev_b32_e32 v59, 16, v58
	v_lshlrev_b32_e32 v58, 16, v106
	s_waitcnt lgkmcnt(0)
	v_pk_fma_f32 v[54:55], v[54:55], v[62:63], v[64:65]
	v_pk_add_f32 v[60:61], v[56:57], v[58:59] neg_lo:[0,1] neg_hi:[0,1]
	v_cvt_pk_bf16_f32 v107, v54, 0
	v_cvt_pk_bf16_f32 v58, v55, 0
	v_lshlrev_b32_e32 v63, 16, v58
	v_lshlrev_b32_e32 v62, 16, v107
	v_pk_add_f32 v[64:65], v[54:55], v[62:63] neg_lo:[0,1] neg_hi:[0,1]
	v_med3_f32 v56, v56, s68, v132
	v_med3_f32 v57, v57, s68, v132
	v_mov_b32_e32 v62, 0
	v_cvt_pk_fp8_f32 v62, v56, v57
	v_med3_f32 v54, v54, s68, v132
	v_med3_f32 v55, v55, s68, v132
	v_and_or_b32 v58, v106, s64, v59
	v_cvt_pk_fp8_f32 v62, v54, v55 op_sel:[0,0,1]
	v_and_or_b32 v59, v107, s64, v63
	v_cvt_pk_bf16_f32 v56, v60, v61
	v_cvt_pk_bf16_f32 v57, v64, v65
	global_store_dwordx2 v[12:13], v[58:59], off offset:2048 sc1
	global_store_dwordx2 v[16:17], v[56:57], off offset:2048 sc1
	global_store_dword v[50:51], v62, off sc1
	v_add_u32_e32 v54, 0x5400, v5
	v_add_u32_e32 v56, 0x7400, v5
	ds_read2_b32 v[54:55], v54 offset1:1
	ds_read2_b32 v[56:57], v56 offset1:1
	v_add_u32_e32 v58, 0x5408, v5
	v_add_u32_e32 v60, 0x7408, v5
	ds_read2_b32 v[58:59], v58 offset1:1
	ds_read2_b32 v[60:61], v60 offset1:1
	v_pk_mul_f32 v[10:11], v[10:11], v[4:5] op_sel_hi:[1,0]
	s_waitcnt lgkmcnt(2)
	v_pk_fma_f32 v[52:53], v[52:53], v[54:55], v[56:57]
	v_pk_mul_f32 v[8:9], v[8:9], v[4:5] op_sel_hi:[1,0]
	v_cvt_pk_bf16_f32 v62, v52, 0
	v_cvt_pk_bf16_f32 v54, v53, 0
	v_lshlrev_b32_e32 v55, 16, v54
	v_lshlrev_b32_e32 v54, 16, v62
	s_waitcnt lgkmcnt(0)
	v_pk_fma_f32 v[14:15], v[14:15], v[58:59], v[60:61]
	v_pk_add_f32 v[56:57], v[52:53], v[54:55] neg_lo:[0,1] neg_hi:[0,1]
	v_cvt_pk_bf16_f32 v63, v14, 0
	v_cvt_pk_bf16_f32 v54, v15, 0
	v_lshlrev_b32_e32 v59, 16, v54
	v_lshlrev_b32_e32 v58, 16, v63
	v_pk_add_f32 v[60:61], v[14:15], v[58:59] neg_lo:[0,1] neg_hi:[0,1]
	v_med3_f32 v52, v52, s68, v132
	v_med3_f32 v53, v53, s68, v132
	v_mov_b32_e32 v58, 0
	v_cvt_pk_fp8_f32 v58, v52, v53
	v_med3_f32 v14, v14, s68, v132
	v_med3_f32 v15, v15, s68, v132
	v_and_or_b32 v54, v62, s64, v55
	v_cvt_pk_fp8_f32 v58, v14, v15 op_sel:[0,0,1]
	v_and_or_b32 v55, v63, s64, v59
	v_cvt_pk_bf16_f32 v52, v56, v57
	v_cvt_pk_bf16_f32 v53, v60, v61
	global_store_dwordx2 v[12:13], v[54:55], off offset:2560 sc1
	global_store_dwordx2 v[16:17], v[52:53], off offset:2560 sc1
	global_store_dword v[50:51], v58, off offset:256 sc1
	v_add_u32_e32 v14, 0x5800, v5
	v_add_u32_e32 v52, 0x7800, v5
	ds_read2_b32 v[14:15], v14 offset1:1
	ds_read2_b32 v[52:53], v52 offset1:1
	v_add_u32_e32 v54, 0x5808, v5
	v_add_u32_e32 v56, 0x7808, v5
	ds_read2_b32 v[54:55], v54 offset1:1
	ds_read2_b32 v[56:57], v56 offset1:1
	v_pk_mul_f32 v[6:7], v[6:7], v[4:5] op_sel_hi:[1,0]
	s_waitcnt lgkmcnt(2)
	v_pk_fma_f32 v[10:11], v[10:11], v[14:15], v[52:53]
	s_add_u32 s12, s12, 0x800
	v_cvt_pk_bf16_f32 v58, v10, 0
	v_cvt_pk_bf16_f32 v14, v11, 0
	v_lshlrev_b32_e32 v15, 16, v14
	v_lshlrev_b32_e32 v14, 16, v58
	s_waitcnt lgkmcnt(0)
	v_pk_fma_f32 v[8:9], v[8:9], v[54:55], v[56:57]
	v_pk_add_f32 v[52:53], v[10:11], v[14:15] neg_lo:[0,1] neg_hi:[0,1]
	v_cvt_pk_bf16_f32 v59, v8, 0
	v_cvt_pk_bf16_f32 v14, v9, 0
	v_lshlrev_b32_e32 v55, 16, v14
	v_lshlrev_b32_e32 v54, 16, v59
	v_pk_add_f32 v[56:57], v[8:9], v[54:55] neg_lo:[0,1] neg_hi:[0,1]
	v_med3_f32 v10, v10, s68, v132
	v_med3_f32 v11, v11, s68, v132
	v_mov_b32_e32 v54, 0
	v_cvt_pk_fp8_f32 v54, v10, v11
	v_med3_f32 v8, v8, s68, v132
	v_med3_f32 v9, v9, s68, v132
	v_and_or_b32 v14, v58, s64, v15
	v_cvt_pk_fp8_f32 v54, v8, v9 op_sel:[0,0,1]
	v_and_or_b32 v15, v59, s64, v55
	v_cvt_pk_bf16_f32 v10, v52, v53
	v_cvt_pk_bf16_f32 v11, v56, v57
	global_store_dwordx2 v[12:13], v[14:15], off offset:3072 sc1
	global_store_dwordx2 v[16:17], v[10:11], off offset:3072 sc1
	global_store_dword v[50:51], v54, off offset:512 sc1
	v_add_u32_e32 v8, 0x5c00, v5
	v_add_u32_e32 v10, 0x7c00, v5
	ds_read2_b32 v[8:9], v8 offset1:1
	ds_read2_b32 v[10:11], v10 offset1:1
	v_add_u32_e32 v14, 0x5c08, v5
	v_add_u32_e32 v5, 0x7c08, v5
	ds_read2_b32 v[14:15], v14 offset1:1
	ds_read2_b32 v[52:53], v5 offset1:1
	s_addc_u32 s13, s13, 0
	s_waitcnt lgkmcnt(2)
	v_pk_fma_f32 v[6:7], v[6:7], v[8:9], v[10:11]
	s_cmp_eq_u32 s10, 0x10000
	v_cvt_pk_bf16_f32 v5, v7, 0
	v_cvt_pk_bf16_f32 v54, v6, 0
	v_pk_mul_f32 v[2:3], v[2:3], v[4:5] op_sel_hi:[1,0]
	v_lshlrev_b32_e32 v9, 16, v5
	v_lshlrev_b32_e32 v8, 16, v54
	s_waitcnt lgkmcnt(0)
	v_pk_fma_f32 v[2:3], v[2:3], v[14:15], v[52:53]
	v_pk_add_f32 v[10:11], v[6:7], v[8:9] neg_lo:[0,1] neg_hi:[0,1]
	v_cvt_pk_bf16_f32 v8, v2, 0
	v_cvt_pk_bf16_f32 v4, v3, 0
	v_lshlrev_b32_e32 v5, 16, v4
	v_lshlrev_b32_e32 v4, 16, v8
	v_pk_add_f32 v[14:15], v[2:3], v[4:5] neg_lo:[0,1] neg_hi:[0,1]
	v_and_or_b32 v5, v8, s64, v5
	v_med3_f32 v6, v6, s68, v132
	v_med3_f32 v7, v7, s68, v132
	v_mov_b32_e32 v8, 0
	v_cvt_pk_fp8_f32 v8, v6, v7
	v_med3_f32 v2, v2, s68, v132
	v_med3_f32 v3, v3, s68, v132
	v_and_or_b32 v4, v54, s64, v9
	v_cvt_pk_fp8_f32 v8, v2, v3 op_sel:[0,0,1]
	v_cvt_pk_bf16_f32 v6, v10, v11
	v_cvt_pk_bf16_f32 v7, v14, v15
	global_store_dwordx2 v[12:13], v[4:5], off offset:3584 sc1
	global_store_dwordx2 v[16:17], v[6:7], off offset:3584 sc1
	global_store_dword v[50:51], v8, off offset:768 sc1
	s_cbranch_scc1 .LBB0_2155
	s_waitcnt vmcnt(32)
	v_mov_b64_e32 v[106:107], v[96:97]
	v_mov_b64_e32 v[108:109], v[98:99]
	v_mov_b64_e32 v[110:111], v[100:101]
	v_mov_b64_e32 v[112:113], v[102:103]
	v_mov_b64_e32 v[114:115], v[88:89]
	v_mov_b64_e32 v[116:117], v[90:91]
	v_mov_b64_e32 v[118:119], v[92:93]
	v_mov_b64_e32 v[120:121], v[94:95]
	v_mov_b32_e32 v62, v18
	v_mov_b32_e32 v63, v19
	v_mov_b32_e32 v64, v20
	v_mov_b32_e32 v65, v21
	v_mov_b32_e32 v58, v22
	v_mov_b32_e32 v59, v23
	v_mov_b32_e32 v60, v24
	v_mov_b32_e32 v61, v25
	v_mov_b32_e32 v54, v26
	v_mov_b32_e32 v55, v27
	v_mov_b32_e32 v56, v28
	v_mov_b32_e32 v57, v29
	v_mov_b32_e32 v14, v30
	v_mov_b32_e32 v15, v31
	v_mov_b32_e32 v16, v32
	v_mov_b32_e32 v17, v33
	v_mov_b32_e32 v50, v34
	v_mov_b32_e32 v51, v35
	v_mov_b32_e32 v52, v36
	v_mov_b32_e32 v53, v37
	v_mov_b32_e32 v10, v38
	v_mov_b32_e32 v11, v39
	v_mov_b32_e32 v12, v40
	v_mov_b32_e32 v13, v41
	v_mov_b32_e32 v6, v42
	v_mov_b32_e32 v7, v43
	v_mov_b32_e32 v8, v44
	v_mov_b32_e32 v9, v45
	v_mov_b32_e32 v2, v46
	v_mov_b32_e32 v3, v47
	v_mov_b32_e32 v4, v48
	v_mov_b32_e32 v5, v49
	s_cmpk_eq_u32 s10, 0xf000
	v_lshl_add_u64 v[122:123], v[82:83], 0, s[10:11]
	s_cbranch_scc0 .Lp10_issue
	s_branch .Lp10_head
